# attention: rescale decision taken on the half-wave row max (cross-half permlane combine only on the rare rescale path)
# speedup vs baseline: 1.0093x; 1.0008x over previous
; __device__ __forceinline__ void partialSM(f32x16& p0, f32x16& p1, float& m_reg, float& alpha, const bool first) {
;     float ma = max3f(p0[0], p0[1], p0[2]), mb = max3f(p0[3], p0[4], p0[5]), mc = max3f(p0[6], p0[7], p0[8]), md = max3f(p0[9], p0[10], p0[11]);
;     ma = max3f(ma, p0[12], p0[13]); mb = max3f(mb, p0[14], p0[15]); mc = max3f(mc, p1[0], p1[1]); md = max3f(md, p1[2], p1[3]);
;     ma = max3f(ma, p1[4], p1[5]); mb = max3f(mb, p1[6], p1[7]); mc = max3f(mc, p1[8], p1[9]); md = max3f(md, p1[10], p1[11]);
;     ma = max3f(ma, p1[12], p1[13]); mb = max3f(mb, p1[14], p1[15]);
;     float pmax = fmaxf(max3f(ma, mb, mc), md);
;     { auto rr = __builtin_amdgcn_permlane32_swap(__float_as_uint(pmax), __float_as_uint(pmax), false, false);
;       pmax = fmaxf(__uint_as_float(rr[0]), __uint_as_float(rr[1])); }
;     const float u = pmax - PSH;
;     if (__builtin_expect(!first && __all(u <= THR2), 1)) { alpha = 1.f; }
;     else { const float dl = first ? u : fmaxf(u, 0.f); alpha = __builtin_amdgcn_exp2f(-dl); m_reg += dl;
; #pragma unroll
;         for (int r = 0; r < 16; ++r) { p0[r] -= dl; p1[r] -= dl; } }
; #pragma unroll
;     for (int r = 0; r < 16; ++r) p0[r] = __builtin_amdgcn_exp2f(p0[r]);
; }
; __device__ __forceinline__ void finishSM(f32x16& p0, f32x16& p1, float alpha, float& l_reg, v8i& pa) {
; #pragma unroll
;     for (int r = 0; r < 16; ++r) p1[r] = __builtin_amdgcn_exp2f(p1[r]);
;     float sa = p0[0] + p0[1], sb = p0[2] + p0[3], sc = p0[4] + p0[5], sd = p0[6] + p0[7];
;     sa += p0[8]; sb += p0[9]; sc += p0[10]; sd += p0[11]; sa += p0[12]; sb += p0[13]; sc += p0[14]; sd += p0[15];
; #pragma unroll
;     for (int r = 0; r < 16; r += 4) { sa += p1[r]; sb += p1[r + 1]; sc += p1[r + 2]; sd += p1[r + 3]; }
;     float ps = (sa + sb) + (sc + sd);
;     { auto rr = __builtin_amdgcn_permlane32_swap(__float_as_uint(ps), __float_as_uint(ps), false, false);
;       ps = __uint_as_float(rr[0]) + __uint_as_float(rr[1]); }
;     l_reg = l_reg * alpha + ps;
; #pragma unroll
;     for (int c = 0; c < 4; ++c) { pa[c] = (int)pk4_fp8(p0[4 * c], p0[4 * c + 1], p0[4 * c + 2], p0[4 * c + 3]);
;         pa[4 + c] = (int)pk4_fp8(p1[4 * c], p1[4 * c + 1], p1[4 * c + 2], p1[4 * c + 3]); }
; }
; __device__ __forceinline__ void qkt(f32x16& p0, f32x16& p1, const float m_reg, const char* Ks, const v8i* q8, int r32, int hi) {
;     { const float ini = PSH - m_reg;
.LBB0_553:
	v_sub_f32_e32 v80, 0x40400000, v180
	v_mov_b32_e32 v81, v80
	v_mov_b32_e32 v82, v80
	v_mov_b32_e32 v83, v80
	v_mov_b32_e32 v84, v80
	v_mov_b32_e32 v85, v80
	v_mov_b32_e32 v86, v80
	v_mov_b32_e32 v87, v80
	v_mov_b32_e32 v88, v80
	v_mov_b32_e32 v89, v80
	v_mov_b32_e32 v90, v80
	v_mov_b32_e32 v91, v80
	v_mov_b32_e32 v92, v80
	v_mov_b32_e32 v93, v80
	v_mov_b32_e32 v94, v80
	v_mov_b32_e32 v95, v80
	v_exp_f32_e32 v228, v64
	v_exp_f32_e32 v230, v65
	s_waitcnt lgkmcnt(0)
	v_mfma_scale_f32_32x32x64_f8f6f4 v[96:111], v[96:103], v[120:127], v[80:95], v201, v200 op_sel_hi:[0,0,0]
	v_exp_f32_e32 v222, v66
	v_exp_f32_e32 v223, v67
	v_exp_f32_e32 v229, v68
	v_exp_f32_e32 v231, v69
	v_exp_f32_e32 v226, v70
	v_exp_f32_e32 v227, v71
	v_add_f32_e32 v64, v215, v216
	v_add_f32_e32 v65, v190, v192
	v_add_f32_e32 v66, v213, v214
	v_add_f32_e32 v67, v195, v212
	v_exp_f32_e32 v224, v72
	v_exp_f32_e32 v225, v73
	v_exp_f32_e32 v184, v74
	v_exp_f32_e32 v217, v75
	v_add_f32_e32 v64, v194, v64
	v_mfma_scale_f32_32x32x64_f8f6f4 v[80:95], v[136:143], v[120:127], v[80:95], v201, v200 op_sel_hi:[0,0,0]
	ds_read_b128 v[136:139], v164 offset:64
	ds_read_b128 v[140:143], v164 offset:80
	ds_read_b128 v[144:147], v164 offset:6720
	ds_read_b128 v[148:151], v164 offset:6736
	v_add_f32_e32 v65, v211, v65
	v_add_f32_e32 v66, v186, v66
	v_add_f32_e32 v67, v187, v67
	v_exp_f32_e32 v220, v76
	v_exp_f32_e32 v221, v77
	v_exp_f32_e32 v218, v78
	v_exp_f32_e32 v219, v79
	v_add_f32_e32 v64, v191, v64
	v_add_f32_e32 v65, v193, v65
	v_add_f32_e32 v66, v188, v66
	v_add_f32_e32 v67, v189, v67
	v_add_f32_e32 v64, v228, v64
	v_add_f32_e32 v65, v230, v65
	v_add_f32_e32 v66, v222, v66
	s_waitcnt lgkmcnt(0)
	v_mfma_scale_f32_32x32x64_f8f6f4 v[96:111], v[136:143], v[128:135], v[96:111], v201, v200 op_sel_hi:[0,0,0]
	v_add_f32_e32 v67, v223, v67
	v_add_f32_e32 v64, v229, v64
	v_add_f32_e32 v65, v231, v65
	v_add_f32_e32 v66, v226, v66
	v_add_f32_e32 v67, v227, v67
	v_add_f32_e32 v64, v224, v64
	v_add_f32_e32 v65, v225, v65
	v_add_f32_e32 v66, v184, v66
	v_add_f32_e32 v67, v217, v67
	v_add_f32_e32 v64, v220, v64
	v_add_f32_e32 v65, v221, v65
	v_add_f32_e32 v66, v218, v66
	v_add_f32_e32 v67, v219, v67
	v_add_f32_e32 v64, v65, v64
	v_add_f32_e32 v65, v66, v67
	v_mfma_scale_f32_32x32x64_f8f6f4 v[80:95], v[144:151], v[128:135], v[80:95], v201, v200 op_sel_hi:[0,0,0]
	ds_read_b128 v[136:139], v164 offset:128
	ds_read_b128 v[140:143], v164 offset:144
	ds_read_b128 v[144:147], v164 offset:6784
	ds_read_b128 v[148:151], v164 offset:6800
	v_add_f32_e32 v182, v65, v64
	v_mov_b32_e32 v183, v182
	v_cvt_pk_fp8_f32 v232, v215, v216
	v_cvt_pk_fp8_f32 v236, v228, v230
	v_cvt_pk_fp8_f32 v233, v213, v214
	v_cvt_pk_fp8_f32 v237, v229, v231
	v_cvt_pk_fp8_f32 v234, v194, v211
	v_cvt_pk_fp8_f32 v238, v224, v225
	v_cvt_pk_fp8_f32 v235, v191, v193
	v_cvt_pk_fp8_f32 v239, v220, v221
	v_permlane32_swap_b32_e32 v182, v183
	s_waitcnt lgkmcnt(0)
	v_mfma_scale_f32_32x32x64_f8f6f4 v[96:111], v[136:143], v[112:119], v[96:111], v201, v200 op_sel_hi:[0,0,0]
	v_cvt_pk_fp8_f32 v232, v190, v192 op_sel:[0,0,1]
	v_cvt_pk_fp8_f32 v236, v222, v223 op_sel:[0,0,1]
	v_cvt_pk_fp8_f32 v233, v195, v212 op_sel:[0,0,1]
	v_cvt_pk_fp8_f32 v237, v226, v227 op_sel:[0,0,1]
	v_cvt_pk_fp8_f32 v234, v186, v187 op_sel:[0,0,1]
	v_cvt_pk_fp8_f32 v238, v184, v217 op_sel:[0,0,1]
	v_cvt_pk_fp8_f32 v235, v188, v189 op_sel:[0,0,1]
	v_cvt_pk_fp8_f32 v239, v218, v219 op_sel:[0,0,1]
	v_mfma_scale_f32_32x32x64_f8f6f4 v[80:95], v[144:151], v[112:119], v[80:95], v201, v200 op_sel_hi:[0,0,0]
	s_mul_i32 s15, s10, 0x5c00
	s_add_i32 s11, s15, 0
	v_add_u32_e32 v64, s11, v161
	v_add_u32_e32 v176, v64, v179
	ds_read_b128 v[144:147], v176 offset:13312
	ds_read_b128 v[148:151], v176 offset:13328
	ds_read_b128 v[136:139], v176 offset:15872
	ds_read_b128 v[140:143], v176 offset:15888
	ds_read_b128 v[72:75], v176 offset:18432
	ds_read_b128 v[76:79], v176 offset:18448
	ds_read_b128 v[64:67], v176 offset:20992
	ds_read_b128 v[68:71], v176 offset:21008
	v_max_f32_e32 v164, v96, v97
	v_max3_f32 v165, v99, v100, v101
	v_max3_f32 v164, v164, v98, v108
	v_max3_f32 v165, v165, v110, v111
	v_max3_f32 v166, v102, v103, v104
	v_max3_f32 v167, v105, v106, v107
	s_waitcnt lgkmcnt(0)
	v_mfma_scale_f32_32x32x64_f8f6f4 v[0:15], v[232:239], v[144:151], v[0:15], v201, v201 op_sel_hi:[0,0,0]
	v_max3_f32 v164, v164, v109, v84
	v_max3_f32 v165, v165, v86, v87
	v_max3_f32 v166, v166, v80, v81
	v_max3_f32 v167, v167, v82, v83
	v_max3_f32 v164, v164, v85, v92
	v_max3_f32 v165, v165, v94, v95
	v_max3_f32 v166, v166, v88, v89
	v_max3_f32 v167, v167, v90, v91
	v_mfma_scale_f32_32x32x64_f8f6f4 v[48:63], v[232:239], v[136:143], v[48:63], v201, v201 op_sel_hi:[0,0,0]
	v_max3_f32 v164, v164, v93, v165
	v_max3_f32 v164, v164, v166, v167
	s_mov_b32 s0, 0x410c551d
	v_cmp_ge_f32_e32 vcc, s0, v164
	s_cmp_eq_u64 vcc, exec
	v_mov_b32_e32 v185, 1.0
	s_cbranch_scc0 .LBB0_570

; __device__ __forceinline__ void partialSM(f32x16& p0, f32x16& p1, float& m_reg, float& alpha, const bool first) {
;     float ma = max3f(p0[0], p0[1], p0[2]), mb = max3f(p0[3], p0[4], p0[5]), mc = max3f(p0[6], p0[7], p0[8]), md = max3f(p0[9], p0[10], p0[11]);
;     ma = max3f(ma, p0[12], p0[13]); mb = max3f(mb, p0[14], p0[15]); mc = max3f(mc, p1[0], p1[1]); md = max3f(md, p1[2], p1[3]);
;     ma = max3f(ma, p1[4], p1[5]); mb = max3f(mb, p1[6], p1[7]); mc = max3f(mc, p1[8], p1[9]); md = max3f(md, p1[10], p1[11]);
;     ma = max3f(ma, p1[12], p1[13]); mb = max3f(mb, p1[14], p1[15]);
;     float pmax = fmaxf(max3f(ma, mb, mc), md);
;     { auto rr = __builtin_amdgcn_permlane32_swap(__float_as_uint(pmax), __float_as_uint(pmax), false, false);
;       pmax = fmaxf(__uint_as_float(rr[0]), __uint_as_float(rr[1])); }
;     const float u = pmax - PSH;
;     if (__builtin_expect(!first && __all(u <= THR2), 1)) { alpha = 1.f; }
;     else { const float dl = first ? u : fmaxf(u, 0.f); alpha = __builtin_amdgcn_exp2f(-dl); m_reg += dl;
; #pragma unroll
;         for (int r = 0; r < 16; ++r) { p0[r] -= dl; p1[r] -= dl; } }
; #pragma unroll
;     for (int r = 0; r < 16; ++r) p0[r] = __builtin_amdgcn_exp2f(p0[r]);
; }
; __device__ __forceinline__ void finishSM(f32x16& p0, f32x16& p1, float alpha, float& l_reg, v8i& pa) {
; #pragma unroll
;     for (int r = 0; r < 16; ++r) p1[r] = __builtin_amdgcn_exp2f(p1[r]);
;     float sa = p0[0] + p0[1], sb = p0[2] + p0[3], sc = p0[4] + p0[5], sd = p0[6] + p0[7];
;     sa += p0[8]; sb += p0[9]; sc += p0[10]; sd += p0[11]; sa += p0[12]; sb += p0[13]; sc += p0[14]; sd += p0[15];
; #pragma unroll
;     for (int r = 0; r < 16; r += 4) { sa += p1[r]; sb += p1[r + 1]; sc += p1[r + 2]; sd += p1[r + 3]; }
;     float ps = (sa + sb) + (sc + sd);
;     { auto rr = __builtin_amdgcn_permlane32_swap(__float_as_uint(ps), __float_as_uint(ps), false, false);
;       ps = __uint_as_float(rr[0]) + __uint_as_float(rr[1]); }
;     l_reg = l_reg * alpha + ps;
; #pragma unroll
;     for (int c = 0; c < 4; ++c) { pa[c] = (int)pk4_fp8(p0[4 * c], p0[4 * c + 1], p0[4 * c + 2], p0[4 * c + 3]);
;         pa[4 + c] = (int)pk4_fp8(p1[4 * c], p1[4 * c + 1], p1[4 * c + 2], p1[4 * c + 3]); }
; }
; __device__ __forceinline__ void qkt(f32x16& p0, f32x16& p1, const float m_reg, const char* Ks, const v8i* q8, int r32, int hi) {
;     { const float ini = PSH - m_reg;
.LBB0_563:
	v_sub_f32_e32 v64, 0x40400000, v180
	v_mov_b32_e32 v65, v64
	v_mov_b32_e32 v66, v64
	v_mov_b32_e32 v67, v64
	v_mov_b32_e32 v68, v64
	v_mov_b32_e32 v69, v64
	v_mov_b32_e32 v70, v64
	v_mov_b32_e32 v71, v64
	v_mov_b32_e32 v72, v64
	v_mov_b32_e32 v73, v64
	v_mov_b32_e32 v74, v64
	v_mov_b32_e32 v75, v64
	v_mov_b32_e32 v76, v64
	v_mov_b32_e32 v77, v64
	v_mov_b32_e32 v78, v64
	v_mov_b32_e32 v79, v64
	v_exp_f32_e32 v231, v80
	v_exp_f32_e32 v233, v81
	s_waitcnt lgkmcnt(0)
	v_mfma_scale_f32_32x32x64_f8f6f4 v[96:111], v[96:103], v[120:127], v[64:79], v201, v200 op_sel_hi:[0,0,0]
	v_exp_f32_e32 v225, v82
	v_exp_f32_e32 v226, v83
	v_exp_f32_e32 v232, v84
	v_exp_f32_e32 v234, v85
	v_exp_f32_e32 v229, v86
	v_exp_f32_e32 v230, v87
	v_add_f32_e32 v80, v216, v215
	v_add_f32_e32 v81, v194, v192
	v_add_f32_e32 v82, v214, v213
	v_add_f32_e32 v83, v212, v211
	v_exp_f32_e32 v227, v88
	v_exp_f32_e32 v228, v89
	v_exp_f32_e32 v219, v90
	v_exp_f32_e32 v220, v91
	v_add_f32_e32 v80, v193, v80
	v_mfma_scale_f32_32x32x64_f8f6f4 v[64:79], v[136:143], v[120:127], v[64:79], v201, v200 op_sel_hi:[0,0,0]
	ds_read_b128 v[136:139], v164 offset:64
	ds_read_b128 v[140:143], v164 offset:80
	ds_read_b128 v[144:147], v164 offset:6720
	ds_read_b128 v[148:151], v164 offset:6736
	v_add_f32_e32 v81, v195, v81
	v_add_f32_e32 v82, v186, v82
	v_add_f32_e32 v83, v187, v83
	v_exp_f32_e32 v223, v92
	v_exp_f32_e32 v224, v93
	v_exp_f32_e32 v221, v94
	v_exp_f32_e32 v222, v95
	v_add_f32_e32 v80, v190, v80
	v_add_f32_e32 v81, v191, v81
	v_add_f32_e32 v82, v188, v82
	v_add_f32_e32 v83, v189, v83
	v_add_f32_e32 v80, v80, v231
	v_add_f32_e32 v81, v81, v233
	v_add_f32_e32 v82, v82, v225
	s_waitcnt lgkmcnt(0)
	v_mfma_scale_f32_32x32x64_f8f6f4 v[96:111], v[136:143], v[128:135], v[96:111], v201, v200 op_sel_hi:[0,0,0]
	v_add_f32_e32 v83, v83, v226
	v_add_f32_e32 v80, v232, v80
	v_add_f32_e32 v81, v234, v81
	v_add_f32_e32 v82, v229, v82
	v_add_f32_e32 v83, v230, v83
	v_add_f32_e32 v80, v227, v80
	v_add_f32_e32 v81, v228, v81
	v_add_f32_e32 v82, v219, v82
	v_add_f32_e32 v83, v220, v83
	v_add_f32_e32 v80, v223, v80
	v_add_f32_e32 v81, v224, v81
	v_add_f32_e32 v82, v221, v82
	v_add_f32_e32 v83, v222, v83
	v_add_f32_e32 v80, v81, v80
	v_add_f32_e32 v81, v82, v83
	v_mfma_scale_f32_32x32x64_f8f6f4 v[64:79], v[144:151], v[128:135], v[64:79], v201, v200 op_sel_hi:[0,0,0]
	ds_read_b128 v[136:139], v164 offset:128
	ds_read_b128 v[140:143], v164 offset:144
	ds_read_b128 v[144:147], v164 offset:6784
	ds_read_b128 v[148:151], v164 offset:6800
	v_add_f32_e32 v217, v81, v80
	v_mov_b32_e32 v218, v217
	v_cvt_pk_fp8_f32 v236, v215, v216
	v_cvt_pk_fp8_f32 v240, v231, v233
	v_cvt_pk_fp8_f32 v237, v213, v214
	v_cvt_pk_fp8_f32 v241, v232, v234
	v_cvt_pk_fp8_f32 v238, v193, v195
	v_cvt_pk_fp8_f32 v242, v227, v228
	v_cvt_pk_fp8_f32 v239, v190, v191
	v_cvt_pk_fp8_f32 v243, v223, v224
	v_permlane32_swap_b32_e32 v217, v218
	s_waitcnt lgkmcnt(0)
	v_mfma_scale_f32_32x32x64_f8f6f4 v[96:111], v[136:143], v[112:119], v[96:111], v201, v200 op_sel_hi:[0,0,0]
	v_cvt_pk_fp8_f32 v236, v192, v194 op_sel:[0,0,1]
	v_cvt_pk_fp8_f32 v240, v225, v226 op_sel:[0,0,1]
	v_cvt_pk_fp8_f32 v237, v211, v212 op_sel:[0,0,1]
	v_cvt_pk_fp8_f32 v241, v229, v230 op_sel:[0,0,1]
	v_cvt_pk_fp8_f32 v238, v186, v187 op_sel:[0,0,1]
	v_cvt_pk_fp8_f32 v242, v219, v220 op_sel:[0,0,1]
	v_cvt_pk_fp8_f32 v239, v188, v189 op_sel:[0,0,1]
	v_cvt_pk_fp8_f32 v243, v221, v222 op_sel:[0,0,1]
	v_mfma_scale_f32_32x32x64_f8f6f4 v[64:79], v[144:151], v[112:119], v[64:79], v201, v200 op_sel_hi:[0,0,0]
	v_add3_u32 v84, s12, v161, v179
	ds_read_b128 v[144:147], v84 offset:13312
	ds_read_b128 v[148:151], v84 offset:13328
	ds_read_b128 v[136:139], v84 offset:15872
	ds_read_b128 v[140:143], v84 offset:15888
	ds_read_b128 v[88:91], v84 offset:18432
	ds_read_b128 v[92:95], v84 offset:18448
	ds_read_b128 v[80:83], v84 offset:20992
	ds_read_b128 v[84:87], v84 offset:21008
	s_nop 2
	v_max_f32_e32 v164, v96, v97
	v_max3_f32 v165, v99, v100, v101
	v_max3_f32 v164, v164, v98, v108
	v_max3_f32 v165, v165, v110, v111
	v_max3_f32 v166, v102, v103, v104
	v_max3_f32 v167, v105, v106, v107
	s_waitcnt lgkmcnt(0)
	v_mfma_scale_f32_32x32x64_f8f6f4 v[0:15], v[236:243], v[144:151], v[0:15], v201, v201 op_sel_hi:[0,0,0]
	v_max3_f32 v164, v164, v109, v68
	v_max3_f32 v165, v165, v70, v71
	v_max3_f32 v166, v166, v64, v65
	v_max3_f32 v167, v167, v66, v67
	v_max3_f32 v164, v164, v69, v76
	v_max3_f32 v165, v165, v78, v79
	v_max3_f32 v166, v166, v72, v73
	v_max3_f32 v167, v167, v74, v75
	v_mfma_scale_f32_32x32x64_f8f6f4 v[48:63], v[236:243], v[136:143], v[48:63], v201, v201 op_sel_hi:[0,0,0]
	v_max3_f32 v164, v164, v77, v165
	v_max3_f32 v164, v164, v166, v167
	s_mov_b32 s0, 0x410c551d
	v_cmp_ge_f32_e32 vcc, s0, v164
	s_cmp_eq_u64 vcc, exec
	v_mov_b32_e32 v184, 1.0
	s_cbranch_scc0 .LBB0_571

; __device__ __forceinline__ void partialSM(f32x16& p0, f32x16& p1, float& m_reg, float& alpha, const bool first) {
;     ...
;     { auto rr = __builtin_amdgcn_permlane32_swap(__float_as_uint(pmax), __float_as_uint(pmax), false, false);
;       pmax = fmaxf(__uint_as_float(rr[0]), __uint_as_float(rr[1])); }
;     const float u = pmax - PSH;
;     if (__builtin_expect(!first && __all(u <= THR2), 1)) { alpha = 1.f; }
;     else { const float dl = first ? u : fmaxf(u, 0.f); alpha = __builtin_amdgcn_exp2f(-dl); m_reg += dl;
; #pragma unroll
;         for (int r = 0; r < 16; ++r) { p0[r] -= dl; p1[r] -= dl; } }
.LBB0_570:
	v_mov_b32_e32 v165, v164
	s_nop 1
	v_permlane32_swap_b32_e32 v164, v165
	v_max_f32_e32 v164, v164, v165
	v_add_f32_e32 v164, 0xc0400000, v164
	v_max_f32_e32 v164, 0, v164
	v_exp_f32_e64 v185, -v164
	v_add_f32_e32 v180, v180, v164
	v_pk_add_f32 v[96:97], v[96:97], v[164:165] op_sel_hi:[1,0] neg_lo:[0,1] neg_hi:[0,1]
	v_pk_add_f32 v[98:99], v[98:99], v[164:165] op_sel_hi:[1,0] neg_lo:[0,1] neg_hi:[0,1]
	v_pk_add_f32 v[100:101], v[100:101], v[164:165] op_sel_hi:[1,0] neg_lo:[0,1] neg_hi:[0,1]
	v_pk_add_f32 v[102:103], v[102:103], v[164:165] op_sel_hi:[1,0] neg_lo:[0,1] neg_hi:[0,1]
	v_pk_add_f32 v[104:105], v[104:105], v[164:165] op_sel_hi:[1,0] neg_lo:[0,1] neg_hi:[0,1]
	v_pk_add_f32 v[106:107], v[106:107], v[164:165] op_sel_hi:[1,0] neg_lo:[0,1] neg_hi:[0,1]
	v_pk_add_f32 v[108:109], v[108:109], v[164:165] op_sel_hi:[1,0] neg_lo:[0,1] neg_hi:[0,1]
	v_pk_add_f32 v[110:111], v[110:111], v[164:165] op_sel_hi:[1,0] neg_lo:[0,1] neg_hi:[0,1]
	v_sub_f32_e32 v95, v95, v164
	v_sub_f32_e32 v94, v94, v164
	v_sub_f32_e32 v93, v93, v164
	v_sub_f32_e32 v92, v92, v164
	v_sub_f32_e32 v91, v91, v164
	v_sub_f32_e32 v90, v90, v164
	v_sub_f32_e32 v89, v89, v164
	v_sub_f32_e32 v88, v88, v164
	v_sub_f32_e32 v87, v87, v164
	v_sub_f32_e32 v86, v86, v164
	v_sub_f32_e32 v85, v85, v164
	v_sub_f32_e32 v84, v84, v164
	v_sub_f32_e32 v83, v83, v164
	v_sub_f32_e32 v82, v82, v164
	v_sub_f32_e32 v81, v81, v164
	v_sub_f32_e32 v80, v80, v164
	s_branch .LBB0_554
.LBB0_571:
	v_mov_b32_e32 v165, v164
	s_nop 1
	v_permlane32_swap_b32_e32 v164, v165
	v_max_f32_e32 v164, v164, v165
	v_add_f32_e32 v164, 0xc0400000, v164
	v_max_f32_e32 v164, 0, v164
	v_exp_f32_e64 v184, -v164
	v_add_f32_e32 v180, v180, v164
	v_pk_add_f32 v[96:97], v[96:97], v[164:165] op_sel_hi:[1,0] neg_lo:[0,1] neg_hi:[0,1]
	v_pk_add_f32 v[98:99], v[98:99], v[164:165] op_sel_hi:[1,0] neg_lo:[0,1] neg_hi:[0,1]
	v_pk_add_f32 v[100:101], v[100:101], v[164:165] op_sel_hi:[1,0] neg_lo:[0,1] neg_hi:[0,1]
	v_pk_add_f32 v[102:103], v[102:103], v[164:165] op_sel_hi:[1,0] neg_lo:[0,1] neg_hi:[0,1]
	v_pk_add_f32 v[104:105], v[104:105], v[164:165] op_sel_hi:[1,0] neg_lo:[0,1] neg_hi:[0,1]
	v_pk_add_f32 v[106:107], v[106:107], v[164:165] op_sel_hi:[1,0] neg_lo:[0,1] neg_hi:[0,1]
	v_pk_add_f32 v[108:109], v[108:109], v[164:165] op_sel_hi:[1,0] neg_lo:[0,1] neg_hi:[0,1]
	v_pk_add_f32 v[110:111], v[110:111], v[164:165] op_sel_hi:[1,0] neg_lo:[0,1] neg_hi:[0,1]
	v_sub_f32_e32 v79, v79, v164
	v_sub_f32_e32 v78, v78, v164
	v_sub_f32_e32 v77, v77, v164
	v_sub_f32_e32 v76, v76, v164
	v_sub_f32_e32 v75, v75, v164
	v_sub_f32_e32 v74, v74, v164
	v_sub_f32_e32 v73, v73, v164
	v_sub_f32_e32 v72, v72, v164
	v_sub_f32_e32 v71, v71, v164
	v_sub_f32_e32 v70, v70, v164
	v_sub_f32_e32 v69, v69, v164
	v_sub_f32_e32 v68, v68, v164
	v_sub_f32_e32 v67, v67, v164
	v_sub_f32_e32 v66, v66, v164
	v_sub_f32_e32 v65, v65, v164
	v_sub_f32_e32 v64, v64, v164
	s_branch .LBB0_564
